# baseline (speedup 1.0000x reference)
.LBB3_36:
	s_andn2_b64 vcc, exec, s[6:7]
	s_cbranch_vccnz .LBB3_86
	s_cmpk_gt_u32 s2, 0xff
	s_cbranch_scc1 .LBB3_86
	s_mov_b64 s[40:41], s[0:1]
	s_mov_b32 s44, s18
	s_mov_b32 s45, s19
	s_mov_b32 s46, 0
	s_mov_b32 s60, s2
	s_mov_b32 s61, 0
	s_mov_b32 s65, 0
	s_mov_b32 s73, 0
	v_readfirstlane_b32 s72, v0
	s_nop 3
	s_cmp_ge_u32 s72, 0x100
	s_cselect_b32 s79, 1, 0
	s_load_dwordx2 s[68:69], s[0:1], 0x0
	s_load_dwordx2 s[70:71], s[0:1], 0x38
	s_mov_b32 s49, 0
	s_mov_b32 s47, 0
	s_mov_b32 s48, 0
	s_movk_i32 s50, 27
	s_load_dwordx2 s[52:53], s[0:1], 0x30
	s_add_i32 s51, s19, 31
	s_lshr_b32 s51, s51, 5
	s_sub_i32 s51, s51, 0x200
	s_sub_i32 s55, s51, 1
	s_cmp_lt_u32 s55, 0x80
	s_cselect_b32 s51, s51, 0
	v_mov_b32_e32 v248, v0

.LBB3_61:
	s_or_b64 exec, exec, s[4:5]
	s_movk_i32 s5, 0x2b0
	v_mov_b32_e32 v5, 0x15000
	v_mad_u32_u24 v206, v0, s5, v5
	v_mov_b32_e32 v5, 0x3c00
	v_cmp_eq_u32_e32 vcc, 0, v55
	s_movk_i32 s4, 0xf0
	v_mul_u32_u24_e32 v3, 56, v55
	v_cndmask_b32_e32 v208, 0, v5, vcc
	v_lshlrev_b32_e32 v5, 3, v204
	v_lshl_or_b32 v5, v195, 8, v5
	v_add_u32_e32 v209, 0x26a80, v5
	v_mov_b32_e32 v5, 0x23800
	v_mov_b32_e32 v2, 0x1fc00
	v_mad_u32_u24 v4, v204, s5, v3
	s_mov_b32 s8, 0x15000
	v_mad_u32_u24 v207, v204, s4, v5
	v_lshlrev_b32_e32 v5, 3, v205
	v_lshlrev_b32_e32 v194, 4, v205
	v_mad_u32_u24 v2, v204, s4, v2
	v_add3_u32 v210, v207, v3, v5
	v_add3_u32 v212, v4, v194, s8
	s_movk_i32 s4, 0x64
	v_mov_b32_e32 v4, 0x25600
	v_mad_u32_u24 v214, v0, s4, v4
	v_add_u32_e32 v0, 48, v210
	v_cmp_gt_u32_e64 s[4:5], 32, v1
	v_add_u32_e32 v211, v2, v194
	v_add3_u32 v217, v2, v3, v5
	v_cndmask_b32_e64 v218, v209, v0, s[4:5]
	v_mul_u32_u24_e32 v0, 0x1c0, v195
	v_or_b32_e32 v0, v0, v1
	v_lshlrev_b32_e32 v0, 4, v0
	v_mov_b32_e32 v1, 0
	v_add_u32_e32 v2, 0x1000, v0
	v_mov_b32_e32 v3, v1
	v_lshl_add_u64 v[196:197], s[0:1], 0, v[0:1]
	v_lshl_add_u64 v[198:199], s[0:1], 0, v[2:3]
	v_add_u32_e32 v2, 0x1400, v0
	v_add_u32_e32 v0, 0x1800, v0
	v_add_u32_e32 v213, 0x26280, v50
	v_lshl_add_u32 v215, v54, 4, v50
	v_lshl_add_u64 v[200:201], s[0:1], 0, v[2:3]
	v_lshl_add_u64 v[202:203], s[0:1], 0, v[0:1]
	v_mov_b32_e32 v0, v1
	v_mov_b32_e32 v2, v1
	v_mov_b32_e32 v4, v1
	v_mov_b32_e32 v5, v1
	v_mov_b32_e32 v6, v1
	v_mov_b32_e32 v7, v1
	v_mov_b32_e32 v8, v1
	v_mov_b32_e32 v9, v1
	v_mov_b32_e32 v10, v1
	v_mov_b32_e32 v11, v1
	v_mov_b32_e32 v12, v1
	v_mov_b64_e32 v[80:81], v[14:15]
	v_mov_b64_e32 v[64:65], v[14:15]
	v_mov_b64_e32 v[48:49], v[14:15]
	s_mov_b32 s14, 0
	s_mov_b32 s21, 0
	v_add_u32_e32 v216, v207, v194
	s_mov_b32 s15, 0x5040100
	s_movk_i32 s18, 0x2a0
	v_mov_b64_e32 v[78:79], v[12:13]
	v_mov_b64_e32 v[76:77], v[10:11]
	v_mov_b64_e32 v[74:75], v[8:9]
	v_mov_b64_e32 v[72:73], v[6:7]
	v_mov_b64_e32 v[70:71], v[4:5]
	v_mov_b64_e32 v[68:69], v[2:3]
	v_mov_b64_e32 v[66:67], v[0:1]
	v_mov_b64_e32 v[62:63], v[12:13]
	v_mov_b64_e32 v[60:61], v[10:11]
	v_mov_b64_e32 v[58:59], v[8:9]
	v_mov_b64_e32 v[56:57], v[6:7]
	v_mov_b64_e32 v[54:55], v[4:5]
	v_mov_b64_e32 v[52:53], v[2:3]
	v_mov_b64_e32 v[50:51], v[0:1]
	v_mov_b64_e32 v[46:47], v[12:13]
	v_mov_b64_e32 v[44:45], v[10:11]
	v_mov_b64_e32 v[42:43], v[8:9]
	v_mov_b64_e32 v[40:41], v[6:7]
	v_mov_b64_e32 v[38:39], v[4:5]
	v_mov_b64_e32 v[36:37], v[2:3]
	v_mov_b64_e32 v[34:35], v[0:1]
	v_mov_b32_e32 v13, v1
	v_mov_b32_e32 v14, v1
	v_mov_b32_e32 v15, v1
	v_mov_b32_e32 v16, v1
	v_mov_b32_e32 v17, v1
	v_mov_b32_e32 v18, v1
	v_mov_b32_e32 v19, v1
	v_mov_b32_e32 v20, v1
	v_mov_b32_e32 v21, v1
	v_mov_b32_e32 v22, v1
	v_mov_b32_e32 v23, v1
	v_mov_b32_e32 v24, v1
	v_mov_b32_e32 v25, v1
	v_mov_b32_e32 v26, v1
	v_mov_b32_e32 v27, v1
	v_mov_b32_e32 v28, v1
	v_mov_b32_e32 v29, v1
	v_mov_b32_e32 v30, v1
	s_cmp_eq_u32 s47, 2
	s_cbranch_scc1 .Lgru_restore
	s_cmp_lt_u32 s72, 0x100
	s_cbranch_scc1 .Lapf_skip_a
	ds_read_b128 v[232:235], v215
	ds_read_b128 v[236:239], v215 offset:7168
	ds_read_b128 v[240:243], v215 offset:14336
	ds_read_b128 v[244:247], v215 offset:1024
	ds_read_b128 v[200:203], v215 offset:8192

.Lpf_done:
	s_add_i32 s14, s14, 1
	s_cmp_eq_u32 s14, s50
	s_waitcnt lgkmcnt(0)
	s_barrier
	s_cbranch_scc1 .LBB3_83
.LBB3_63:
	s_cmp_eq_u32 s79, 0
	s_cbranch_scc1 .LBB3_66
	v_add_u32_e32 v231, s21, v211
	ds_read_b128 v[166:169], v231
	s_cmp_lt_u32 s14, 2
	s_cbranch_scc1 .Lgru_l1_mid
	v_exp_f32_e32 v0, v2
	v_exp_f32_e32 v2, v3
	v_exp_f32_e32 v3, v4
	v_exp_f32_e32 v4, v5
	v_exp_f32_e32 v5, v6
	v_exp_f32_e32 v6, v7
	v_exp_f32_e32 v7, v8
	v_exp_f32_e32 v8, v9
	v_exp_f32_e32 v9, v10
	v_exp_f32_e32 v10, v11
	v_exp_f32_e32 v11, v12
	v_exp_f32_e32 v12, v13
	v_exp_f32_e32 v13, v14
	v_add_f32_e32 v0, 1.0, v0
	v_exp_f32_e32 v14, v18
	v_exp_f32_e32 v18, v19
	v_exp_f32_e32 v19, v20
	v_exp_f32_e32 v20, v21
	v_exp_f32_e32 v21, v22
	v_exp_f32_e32 v22, v23
	v_exp_f32_e32 v23, v24
	v_exp_f32_e32 v24, v25
	v_exp_f32_e32 v25, v26
	v_exp_f32_e32 v26, v27
	v_exp_f32_e32 v27, v28
	v_exp_f32_e32 v28, v29
	v_exp_f32_e32 v29, v30
	v_add_f32_e32 v30, 1.0, v2
	v_add_f32_e32 v65, 1.0, v11
	v_rcp_f32_e32 v2, v0
	v_add_f32_e32 v79, 1.0, v12
	v_rcp_f32_e32 v12, v65
	v_add_f32_e32 v31, 1.0, v3
	v_rcp_f32_e32 v3, v30
	v_add_f32_e32 v47, 1.0, v6
	v_add_f32_e32 v80, 1.0, v13
	v_rcp_f32_e32 v13, v79
	v_add_f32_e32 v32, 1.0, v4
	v_add_f32_e32 v48, 1.0, v7
	v_rcp_f32_e32 v4, v31
	v_rcp_f32_e32 v7, v47
	v_fma_f32 v0, v2, v34, v66
	v_add_f32_e32 v81, 1.0, v14
	v_rcp_f32_e32 v14, v80
	v_fma_f32 v66, v12, v44, v76
	v_exp_f32_e32 v0, v0
	v_add_f32_e32 v33, 1.0, v5
	v_add_f32_e32 v49, 1.0, v8
	v_rcp_f32_e32 v5, v32
	v_rcp_f32_e32 v8, v48
	v_fma_f32 v31, v3, v35, v67
	v_exp_f32_e32 v66, v66
	v_fma_f32 v67, v13, v45, v77
	v_exp_f32_e32 v31, v31
	v_rcp_f32_e32 v6, v33
	v_fma_f32 v32, v4, v36, v68
	v_fma_f32 v48, v7, v39, v71
	v_exp_f32_e32 v67, v67
	v_fma_f32 v68, v14, v46, v78
	v_exp_f32_e32 v32, v32
	v_exp_f32_e32 v48, v48
	v_add_f32_e32 v0, 1.0, v0
	v_add_f32_e32 v63, 1.0, v9
	v_rcp_f32_e32 v9, v49
	v_fma_f32 v33, v5, v37, v69
	v_fma_f32 v49, v8, v40, v72
	v_exp_f32_e32 v68, v68
	v_add_f32_e32 v76, 1.0, v66
	v_rcp_f32_e32 v66, v0
	v_exp_f32_e32 v33, v33
	v_exp_f32_e32 v49, v49
	v_add_f32_e32 v31, 1.0, v31
	v_fma_f32 v47, v6, v38, v70
	v_add_f32_e32 v77, 1.0, v67
	v_rcp_f32_e32 v67, v31
	v_add_f32_e32 v219, 1.0, v18
	v_rcp_f32_e32 v18, v81
	v_exp_f32_e32 v47, v47
	v_add_f32_e32 v32, 1.0, v32
	v_add_f32_e32 v48, 1.0, v48
	v_add_f32_e32 v78, 1.0, v68
	v_rcp_f32_e32 v68, v32
	v_rcp_f32_e32 v71, v48
	v_fma_f32 v66, v66, -2.0, 1.0
	v_add_f32_e32 v220, 1.0, v19
	v_rcp_f32_e32 v19, v219
	v_add_f32_e32 v33, 1.0, v33
	v_add_f32_e32 v49, 1.0, v49
	v_add_f32_e32 v64, 1.0, v10
	v_sub_f32_e32 v0, v50, v66
	v_rcp_f32_e32 v10, v63
	v_rcp_f32_e32 v69, v33
	v_rcp_f32_e32 v72, v49
	v_fma_f32 v67, v67, -2.0, 1.0
	v_add_f32_e32 v221, 1.0, v20
	v_rcp_f32_e32 v20, v220
	v_add_f32_e32 v47, 1.0, v47
	v_fma_f32 v50, v18, v0, v66
	v_rcp_f32_e32 v11, v64
	v_sub_f32_e32 v0, v51, v67
	v_fma_f32 v63, v9, v41, v73
	v_rcp_f32_e32 v70, v47
	v_fma_f32 v68, v68, -2.0, 1.0
	v_add_f32_e32 v222, 1.0, v21
	v_rcp_f32_e32 v21, v221
	v_exp_f32_e32 v63, v63
	v_fma_f32 v51, v19, v0, v67
	v_fma_f32 v64, v10, v42, v74
	v_sub_f32_e32 v0, v52, v68
	v_fma_f32 v69, v69, -2.0, 1.0
	v_add_f32_e32 v223, 1.0, v22
	v_rcp_f32_e32 v22, v222
	v_exp_f32_e32 v64, v64
	v_fma_f32 v52, v20, v0, v68
	v_fma_f32 v65, v11, v43, v75
	v_sub_f32_e32 v0, v53, v69
	v_fma_f32 v70, v70, -2.0, 1.0
	v_add_f32_e32 v224, 1.0, v23
	v_rcp_f32_e32 v23, v223
	v_exp_f32_e32 v65, v65
	v_add_f32_e32 v63, 1.0, v63
	v_fma_f32 v53, v21, v0, v69
	v_rcp_f32_e32 v73, v63
	v_sub_f32_e32 v0, v54, v70
	v_fma_f32 v71, v71, -2.0, 1.0
	v_add_f32_e32 v225, 1.0, v24
	v_rcp_f32_e32 v24, v224
	v_add_f32_e32 v64, 1.0, v64
	v_fma_f32 v54, v22, v0, v70
	v_rcp_f32_e32 v74, v64
	v_sub_f32_e32 v0, v55, v71
	v_fma_f32 v72, v72, -2.0, 1.0
	v_add_f32_e32 v226, 1.0, v25
	v_rcp_f32_e32 v25, v225
	v_add_f32_e32 v65, 1.0, v65
	v_fma_f32 v55, v23, v0, v71
	v_rcp_f32_e32 v75, v65
	v_sub_f32_e32 v0, v56, v72
	v_fma_f32 v73, v73, -2.0, 1.0
	v_add_f32_e32 v227, 1.0, v26
	v_rcp_f32_e32 v26, v226
	v_fma_f32 v56, v24, v0, v72
	v_rcp_f32_e32 v76, v76
	v_sub_f32_e32 v0, v57, v73
	v_fma_f32 v74, v74, -2.0, 1.0
	v_add_f32_e32 v228, 1.0, v27
	v_rcp_f32_e32 v27, v227
	v_fma_f32 v57, v25, v0, v73
	v_rcp_f32_e32 v77, v77
	v_sub_f32_e32 v0, v58, v74
	v_fma_f32 v75, v75, -2.0, 1.0
	v_add_f32_e32 v229, 1.0, v28
	v_rcp_f32_e32 v28, v228
	v_fma_f32 v58, v26, v0, v74
	v_rcp_f32_e32 v78, v78
	v_sub_f32_e32 v0, v59, v75
	v_fma_f32 v76, v76, -2.0, 1.0
	v_add_f32_e32 v230, 1.0, v29
	v_rcp_f32_e32 v29, v229
	v_fma_f32 v59, v27, v0, v75
	v_rcp_f32_e32 v30, v230
	v_sub_f32_e32 v0, v60, v76
	v_fma_f32 v77, v77, -2.0, 1.0
	v_fma_f32 v60, v28, v0, v76
	v_fma_f32 v78, v78, -2.0, 1.0
	v_sub_f32_e32 v0, v61, v77
	s_nop 0
	v_fma_f32 v61, v29, v0, v77
	v_sub_f32_e32 v0, v62, v78
	s_nop 0
	v_fma_f32 v62, v30, v0, v78
	v_cvt_pk_f16_f32 v33, v52, v53
	v_cvt_f16_f32_e32 v0, v62
	v_cvt_pk_f16_f32 v32, v50, v51
	v_cvt_pk_f16_f32 v49, v56, v57
	v_cvt_pk_f16_f32 v48, v54, v55
	ds_write2_b64 v210, v[32:33], v[48:49] offset1:2
	v_cvt_pk_f16_f32 v33, v60, v61
	v_cvt_pk_f16_f32 v32, v58, v59
	v_perm_b32 v0, v208, v0, s15
	ds_write_b64 v210, v[32:33] offset:32
	ds_write_b64 v218, v[0:1]
.Lgru_l1_mid:
	s_waitcnt lgkmcnt(0)
	s_barrier
	s_xor_b32 s21, s21, 0x1e00
	s_sub_i32 s8, s14, 1
	s_cmp_gt_u32 s8, 24
	s_cbranch_scc1 .LBB3_62
	s_branch .Lgru_l1_mfma

.LBB3_83:
	s_cmp_eq_u32 s47, 1
	s_cbranch_scc1 .Lgru_dump
	s_and_saveexec_b64 s[0:1], s[2:3]
	s_cbranch_execz .Lgru_tile_end
	v_lshl_add_u32 v50, v205, 4, v207
	ds_read_b128 v[30:33], v50
	ds_read_b128 v[46:49], v50 offset:32
	s_waitcnt vmcnt(6) lgkmcnt(1)
	v_mfma_f32_32x32x16_f16 v[30:45], v[2:5], v[30:33], 0
	s_waitcnt vmcnt(5) lgkmcnt(0)
	v_mfma_f32_32x32x16_f16 v[30:45], v[6:9], v[46:49], v[30:45]
	ds_read_b128 v[0:3], v50 offset:64
	ds_read_b128 v[4:7], v50 offset:96
	s_waitcnt vmcnt(4) lgkmcnt(1)
	v_mfma_f32_32x32x16_f16 v[30:45], v[10:13], v[0:3], v[30:45]
	s_waitcnt vmcnt(3) lgkmcnt(0)
	v_mfma_f32_32x32x16_f16 v[30:45], v[14:17], v[4:7], v[30:45]
	ds_read_b128 v[0:3], v50 offset:128
	ds_read_b128 v[4:7], v50 offset:160
	s_waitcnt vmcnt(2) lgkmcnt(1)
	v_mfma_f32_32x32x16_f16 v[30:45], v[18:21], v[0:3], v[30:45]
	v_mov_b32_e32 v0, 0x27280
	v_lshl_or_b32 v0, v204, 2, v0
	v_mov_b32_e32 v1, 0
	s_waitcnt vmcnt(1) lgkmcnt(0)
	v_mfma_f32_32x32x16_f16 v[30:45], v[22:25], v[4:7], v[30:45]
	ds_read_b32 v0, v0
	ds_read_b128 v[2:5], v50 offset:192
	s_waitcnt lgkmcnt(1)
	v_cmp_lt_i32_e32 vcc, -1, v0
	s_waitcnt vmcnt(0) lgkmcnt(0)
	v_mfma_f32_32x32x16_f16 v[30:45], v[26:29], v[2:5], v[30:45]
	s_and_b64 exec, exec, vcc
	s_cbranch_execz .Lgru_tile_end
	s_movk_i32 s0, 0xfa0
	v_add_u32_e32 v2, 0x7530, v0
	v_cmp_gt_u32_e32 vcc, s0, v0
	s_nop 1
	v_cndmask_b32_e32 v0, v2, v0, vcc
	v_lshlrev_b64 v[2:3], 8, v[0:1]
	v_lshl_add_u64 v[2:3], s[16:17], 0, v[2:3]
	v_lshlrev_b32_e32 v0, 7, v195
	v_lshl_add_u64 v[2:3], v[2:3], 0, v[0:1]
	v_mov_b32_e32 v195, v1
	v_lshl_add_u64 v[0:1], v[2:3], 0, v[194:195]
	global_store_dwordx4 v[0:1], v[30:33], off
	global_store_dwordx4 v[0:1], v[34:37], off offset:32
	global_store_dwordx4 v[0:1], v[38:41], off offset:64
	global_store_dwordx4 v[0:1], v[42:45], off offset:96
.Lgru_tile_end:
	s_mov_b64 exec, -1
	s_add_i32 s49, s49, 1
	s_mov_b32 s47, 0
	s_mov_b32 s48, 0
	s_movk_i32 s50, 27
	s_cmp_lg_u32 s51, 0
	s_cbranch_scc1 .Lgru_sched_split
	s_addk_i32 s44, 0x2000
	s_cmp_lt_i32 s44, s45
	s_cbranch_scc0 .LBB3_86
	s_branch .Lgru_next_tile

.Lgru_rs_r3:
	v_add_u32_e32 v220, 0x400, v248
	v_min_u32_e32 v220, 0x59f, v220
	v_lshlrev_b32_e32 v220, 4, v220
	v_add_u32_e32 v221, 0x18000, v219
	v_add_u32_e32 v222, 0x1a000, v219
	v_add_u32_e32 v223, 0x18000, v220
	global_load_dwordx4 v[224:227], v221, s[58:59] sc0 sc1
	global_load_dwordx4 v[228:231], v222, s[58:59] sc0 sc1
	global_load_dwordx4 v[232:235], v223, s[58:59] sc0 sc1
	v_add_u32_e32 v221, 0x1fc00, v219
	v_add_u32_e32 v222, 0x1fc00, v220
	s_waitcnt vmcnt(2)
	ds_write_b128 v221, v[224:227]
	s_waitcnt vmcnt(1)
	ds_write_b128 v221, v[228:231] offset:8192
	s_waitcnt vmcnt(0)
	ds_write_b128 v222, v[232:235]
	s_movk_i32 s14, 16
	s_mov_b32 s21, 0
	s_cmp_lt_u32 s72, 0x100
	s_cbranch_scc1 .Lapf_skip_b
	ds_read_b128 v[232:235], v215
	ds_read_b128 v[236:239], v215 offset:7168
	ds_read_b128 v[240:243], v215 offset:14336
	ds_read_b128 v[244:247], v215 offset:1024
	ds_read_b128 v[200:203], v215 offset:8192
